# speedup vs baseline: 1.0020x; 1.0020x over previous
_Z11gemm_kernelILi128ELi192ELi1EEv8GemmArgs:
	s_load_dwordx2 s[4:5], s[0:1], 0x38
	s_addk_i32 s2, 0xe0
	s_mov_b32 s3, 0
	s_lshl_b64 s[6:7], s[2:3], 2
	s_waitcnt lgkmcnt(0)
	s_add_u32 s4, s4, s6
	s_addc_u32 s5, s5, s7
	s_load_dword s8, s[4:5], 0x0
	s_waitcnt lgkmcnt(0)
	s_cmp_lt_i32 s8, 0
	s_cbranch_scc1 .LBB3_4
	s_load_dwordx2 s[6:7], s[0:1], 0x48
	s_load_dwordx2 s[4:5], s[0:1], 0x0
	v_lshlrev_b32_e32 v64, 4, v0
	v_and_b32_e32 v1, 32, v0
	v_bitop3_b32 v1, v64, v1, 48 bitop3:0x6c
	s_and_b32 s2, s8, 0xffff
	v_bfe_u32 v4, v0, 2, 4
	v_lshrrev_b32_e32 v2, 1, v0
	v_lshrrev_b32_e32 v1, 1, v1
	v_lshrrev_b32_e32 v6, 3, v0
	v_and_or_b32 v1, v2, 32, v1
	v_add_u32_e32 v5, s2, v4
	v_and_b32_e32 v7, 48, v6
	s_movk_i32 s10, 0x70
	v_add_lshl_u32 v22, v5, v7, 12
	v_mov_b32_e32 v23, 0
	v_lshlrev_b32_e32 v44, 1, v1
	v_bitop3_b32 v1, v6, s10, 64 bitop3:0xc8
	s_waitcnt lgkmcnt(0)
	v_lshl_add_u64 v[2:3], s[4:5], 0, v[22:23]
	v_mov_b32_e32 v45, v23
	v_add_lshl_u32 v48, v5, v1, 12
	v_mov_b32_e32 v49, v23
	s_lshr_b32 s10, s8, 24
	s_bfe_u32 s9, s8, 0x80010
	v_lshl_add_u64 v[46:47], v[2:3], 0, v[44:45]
	v_lshl_add_u64 v[2:3], s[4:5], 0, v[48:49]
	s_mulk_i32 s10, 0x300
	v_lshl_add_u64 v[50:51], v[2:3], 0, v[44:45]
	s_mul_i32 s8, s9, 0xc0
	v_or_b32_e32 v2, s10, v4
	v_add_u32_e32 v4, s8, v2
	v_or_b32_e32 v2, v4, v7
	v_lshlrev_b32_e32 v52, 12, v2
	v_mov_b32_e32 v53, v23
	v_lshl_add_u64 v[2:3], s[6:7], 0, v[52:53]
	v_add_lshl_u32 v56, v4, v1, 12
	v_mov_b32_e32 v57, v23
	v_lshl_add_u64 v[54:55], v[2:3], 0, v[44:45]
	v_lshl_add_u64 v[2:3], s[6:7], 0, v[56:57]
	v_add_u32_e32 v60, 0x80000, v52
	v_mov_b32_e32 v61, v23
	v_lshl_add_u64 v[58:59], v[2:3], 0, v[44:45]
	v_lshl_add_u64 v[2:3], s[6:7], 0, v[60:61]
	v_lshl_add_u64 v[62:63], v[2:3], 0, v[44:45]
	v_readfirstlane_b32 s16, v0
	s_load_dwordx2 s[0:1], s[0:1], 0x98
	s_lshr_b32 s16, s16, 6
	s_lshl_b32 s16, s16, 10
	v_bfe_u32 v1, v0, 6, 2
	v_lshrrev_b32_e32 v80, 2, v0
	s_add_u32 m0, s16, 0
	s_nop 0
	global_load_lds_dwordx4 v[46:47], off
	s_add_u32 m0, s16, 8192
	s_nop 0
	global_load_lds_dwordx4 v[50:51], off
	s_add_u32 m0, s16, 16384
	s_nop 0
	global_load_lds_dwordx4 v[54:55], off
	s_add_u32 m0, s16, 24576
	s_nop 0
	global_load_lds_dwordx4 v[58:59], off
	s_add_u32 m0, s16, 32768
	s_nop 0
	global_load_lds_dwordx4 v[62:63], off
	s_add_u32 m0, s16, 40832
	s_nop 0
	global_load_lds_dwordx4 v[46:47], off offset:128
	s_add_u32 m0, s16, 49024
	s_nop 0
	global_load_lds_dwordx4 v[50:51], off offset:128
	s_add_u32 m0, s16, 57216
	s_nop 0
	global_load_lds_dwordx4 v[54:55], off offset:128
	s_add_u32 m0, s16, 65408
	s_nop 0
	global_load_lds_dwordx4 v[58:59], off offset:128
	s_add_u32 m0, s16, 73600
	s_nop 0
	global_load_lds_dwordx4 v[62:63], off offset:128
	s_mov_b32 s17, 0
	s_mov_b32 s18, 0xa000
	s_mov_b32 s19, 0x14000
	v_lshlrev_b32_e32 v25, 6, v0
	v_lshlrev_b32_e32 v27, 2, v0
	v_and_b32_e32 v24, 48, v0
	v_and_b32_e32 v25, 0x3c0, v25
	v_and_b32_e32 v27, 32, v27
	v_or_b32_e32 v26, v25, v24
	v_bitop3_b32 v87, v25, v27, v24 bitop3:0x36
	v_or_b32_e32 v24, v44, v60
	v_mov_b32_e32 v25, v23
	v_lshl_add_u64 v[24:25], s[6:7], 0, v[24:25]
	s_mov_b64 s[10:11], 0x100
	v_lshl_add_u64 v[70:71], v[24:25], 0, s[10:11]
	v_or_b32_e32 v24, v56, v44
	v_mov_b32_e32 v25, v23
	v_lshl_add_u64 v[24:25], s[6:7], 0, v[24:25]
	v_lshl_add_u64 v[72:73], v[24:25], 0, s[10:11]
	v_or_b32_e32 v24, v52, v44
	v_mov_b32_e32 v25, v23
	v_lshl_add_u64 v[24:25], s[6:7], 0, v[24:25]
	v_lshl_add_u64 v[74:75], v[24:25], 0, s[10:11]
	v_or_b32_e32 v24, v48, v44
	v_mov_b32_e32 v25, v23
	v_lshl_add_u64 v[24:25], s[4:5], 0, v[24:25]
	v_or_b32_e32 v22, v22, v44
	v_and_b32_e32 v81, 64, v80
	v_mul_u32_u24_e32 v86, 0x1800, v1
	v_lshl_add_u64 v[76:77], v[24:25], 0, s[10:11]
	v_lshl_add_u64 v[24:25], s[4:5], 0, v[22:23]
	v_bitop3_b32 v82, v26, v86, v27 bitop3:0xde
	v_lshlrev_b32_e32 v88, 7, v81
	v_lshl_add_u64 v[78:79], v[24:25], 0, s[10:11]
	s_mov_b64 s[4:5], 0
	v_mov_b32_e32 v22, v23
	v_mov_b32_e32 v24, v23
	v_mov_b32_e32 v25, v23
	v_mov_b32_e32 v50, v23
	v_mov_b32_e32 v51, v23
	v_mov_b32_e32 v52, v23
	v_mov_b32_e32 v54, v23
	v_mov_b32_e32 v55, v23
	v_mov_b32_e32 v56, v23
	v_mov_b32_e32 v58, v23
	v_mov_b32_e32 v59, v23
	v_mov_b32_e32 v60, v23
	v_mov_b32_e32 v66, v23
	v_mov_b32_e32 v67, v23
	v_mov_b32_e32 v68, v23
	v_mov_b32_e32 v69, v23
	v_mov_b32_e32 v62, v23
	v_mov_b32_e32 v63, v23
	v_mov_b32_e32 v64, v23
	v_mov_b32_e32 v65, v23
	v_mov_b32_e32 v42, v23
	v_mov_b32_e32 v43, v23
	v_mov_b32_e32 v44, v23
	v_mov_b32_e32 v46, v23
	v_mov_b32_e32 v47, v23
	v_mov_b32_e32 v48, v23
	v_mov_b32_e32 v30, v23
	v_mov_b32_e32 v31, v23
	v_mov_b32_e32 v32, v23
	v_mov_b32_e32 v33, v23
	v_mov_b32_e32 v34, v23
	v_mov_b32_e32 v35, v23
	v_mov_b32_e32 v36, v23
	v_mov_b32_e32 v37, v23
	v_mov_b32_e32 v38, v23
	v_mov_b32_e32 v39, v23
	v_mov_b32_e32 v40, v23
	v_mov_b32_e32 v41, v23
	v_mov_b32_e32 v26, v23
	v_mov_b32_e32 v27, v23
	v_mov_b32_e32 v28, v23
	v_mov_b32_e32 v29, v23
	s_waitcnt vmcnt(5) lgkmcnt(0)
	s_barrier
	v_mov_b32_e32 v20, v87
	v_add_u32_e32 v21, v20, v88
	v_add_u32_e32 v20, v20, v86
	ds_read_b128 v[90:93], v21
	ds_read_b128 v[94:97], v21 offset:2048
	ds_read_b128 v[98:101], v21 offset:4096
	ds_read_b128 v[102:105], v21 offset:6144
	ds_read_b128 v[106:109], v20 offset:16384
	ds_read_b128 v[110:113], v20 offset:18432
	ds_read_b128 v[114:117], v20 offset:20480
	s_nop 0
	s_nop 0
	s_nop 0
	s_nop 0
	s_nop 0
.Ldn_loop:
	s_mov_b32 s7, s17
	v_or_b32_e32 v89, s7, v87
	v_add_u32_e32 v122, v89, v88
	s_add_u32 s6, s19, s16
	s_mov_b32 m0, s6
	v_lshl_add_u64 v[2:3], v[78:79], 0, s[4:5]
	global_load_lds_dwordx4 v[2:3], off
	s_waitcnt lgkmcnt(2)
	v_mfma_f32_16x16x32_f16 v[22:25], v[90:93], v[106:109], v[22:25]
	s_waitcnt lgkmcnt(1)
	v_mfma_f32_16x16x32_f16 v[50:53], v[90:93], v[110:113], v[50:53]
	s_waitcnt lgkmcnt(0)
	v_mfma_f32_16x16x32_f16 v[54:57], v[90:93], v[114:117], v[54:57]
	s_add_u32 m0, s6, 8192
	v_lshl_add_u64 v[4:5], v[76:77], 0, s[4:5]
	global_load_lds_dwordx4 v[4:5], off
	v_mfma_f32_16x16x32_f16 v[58:61], v[94:97], v[106:109], v[58:61]
	v_mfma_f32_16x16x32_f16 v[66:69], v[94:97], v[110:113], v[66:69]
	v_mfma_f32_16x16x32_f16 v[62:65], v[94:97], v[114:117], v[62:65]
	ds_read_b128 v[12:15], v122 offset:1024
	ds_read_b128 v[16:19], v122 offset:3072
	ds_read_b128 v[118:121], v122 offset:5120
	ds_read_b128 v[122:125], v122 offset:7168
	v_add_u32_e32 v134, s7, v82
	ds_read_b128 v[126:129], v134 offset:17408
	ds_read_b128 v[130:133], v134 offset:19456
	ds_read_b128 v[134:137], v134 offset:21504
	s_add_u32 m0, s6, 16384
	v_lshl_add_u64 v[6:7], v[74:75], 0, s[4:5]
	global_load_lds_dwordx4 v[6:7], off
	v_mfma_f32_16x16x32_f16 v[42:45], v[98:101], v[106:109], v[42:45]
	v_mfma_f32_16x16x32_f16 v[46:49], v[98:101], v[110:113], v[46:49]
	v_mfma_f32_16x16x32_f16 v[30:33], v[98:101], v[114:117], v[30:33]
	s_add_u32 m0, s6, 24576
	v_lshl_add_u64 v[8:9], v[72:73], 0, s[4:5]
	global_load_lds_dwordx4 v[8:9], off
	v_mfma_f32_16x16x32_f16 v[34:37], v[102:105], v[106:109], v[34:37]
	v_mfma_f32_16x16x32_f16 v[38:41], v[102:105], v[110:113], v[38:41]
	v_mfma_f32_16x16x32_f16 v[26:29], v[102:105], v[114:117], v[26:29]
	s_add_u32 m0, s6, 32768
	v_lshl_add_u64 v[10:11], v[70:71], 0, s[4:5]
	global_load_lds_dwordx4 v[10:11], off
	s_waitcnt vmcnt(5) lgkmcnt(0)
	s_barrier
	s_mov_b32 s20, s17
	s_mov_b32 s17, s18
	s_mov_b32 s18, s19
	s_mov_b32 s19, s20
	v_or_b32_e32 v20, s17, v87
	v_add_u32_e32 v21, v20, v88
	v_add_u32_e32 v20, v20, v86
	ds_read_b128 v[90:93], v21
	ds_read_b128 v[94:97], v21 offset:2048
	ds_read_b128 v[98:101], v21 offset:4096
	ds_read_b128 v[102:105], v21 offset:6144
	ds_read_b128 v[106:109], v20 offset:16384
	ds_read_b128 v[110:113], v20 offset:18432
	ds_read_b128 v[114:117], v20 offset:20480
	v_mfma_f32_16x16x32_f16 v[22:25], v[12:15], v[126:129], v[22:25]
	v_mfma_f32_16x16x32_f16 v[50:53], v[12:15], v[130:133], v[50:53]
	v_mfma_f32_16x16x32_f16 v[54:57], v[12:15], v[134:137], v[54:57]
	v_mfma_f32_16x16x32_f16 v[58:61], v[16:19], v[126:129], v[58:61]
	v_mfma_f32_16x16x32_f16 v[66:69], v[16:19], v[130:133], v[66:69]
	v_mfma_f32_16x16x32_f16 v[62:65], v[16:19], v[134:137], v[62:65]
	v_mfma_f32_16x16x32_f16 v[42:45], v[118:121], v[126:129], v[42:45]
	v_mfma_f32_16x16x32_f16 v[46:49], v[118:121], v[130:133], v[46:49]
	v_mfma_f32_16x16x32_f16 v[30:33], v[118:121], v[134:137], v[30:33]
	v_mfma_f32_16x16x32_f16 v[34:37], v[122:125], v[126:129], v[34:37]
	v_mfma_f32_16x16x32_f16 v[38:41], v[122:125], v[130:133], v[38:41]
	v_mfma_f32_16x16x32_f16 v[26:29], v[122:125], v[134:137], v[26:29]
	s_add_i32 s3, s3, 1
	s_add_u32 s4, s4, 0x80
	s_addc_u32 s5, s5, 0
	s_cmpk_eq_i32 s4, 0xf00
	s_cbranch_scc0 .Ldn_loop
	v_add_u32_e32 v78, v87, v88
	ds_read_b128 v[70:73], v78 offset:2048
	ds_read_b128 v[74:77], v78 offset:4096
	ds_read_b128 v[86:89], v78 offset:6144
	ds_read_b128 v[90:93], v82 offset:16384
	ds_read_b128 v[94:97], v82 offset:18432
	ds_read_b128 v[98:101], v78
	ds_read_b128 v[102:105], v82 offset:20480
	s_waitcnt lgkmcnt(1)
	v_mfma_f32_16x16x32_f16 v[22:25], v[98:101], v[90:93], v[22:25]
	v_mfma_f32_16x16x32_f16 v[50:53], v[98:101], v[94:97], v[50:53]
	s_waitcnt lgkmcnt(0)
	v_mfma_f32_16x16x32_f16 v[18:21], v[98:101], v[102:105], v[54:57]
	v_mfma_f32_16x16x32_f16 v[54:57], v[70:73], v[90:93], v[58:61]
	v_mfma_f32_16x16x32_f16 v[58:61], v[70:73], v[94:97], v[66:69]
	v_mfma_f32_16x16x32_f16 v[14:17], v[70:73], v[102:105], v[62:65]
	s_nop 2
	ds_read_b128 v[62:65], v78 offset:3072
	ds_read_b128 v[66:69], v78 offset:5120
	ds_read_b128 v[70:73], v78 offset:7168
	ds_read_b128 v[98:101], v82 offset:17408
	ds_read_b128 v[106:109], v82 offset:19456
	ds_read_b128 v[110:113], v78 offset:1024
	ds_read_b128 v[114:117], v82 offset:21504
	v_mfma_f32_16x16x32_f16 v[42:45], v[74:77], v[90:93], v[42:45]
	s_mov_b32 s3, 0xe000
	v_mfma_f32_16x16x32_f16 v[46:49], v[74:77], v[94:97], v[46:49]
	v_mfma_f32_16x16x32_f16 v[10:13], v[74:77], v[102:105], v[30:33]
	v_mfma_f32_16x16x32_f16 v[30:33], v[86:89], v[90:93], v[34:37]
	v_mfma_f32_16x16x32_f16 v[34:37], v[86:89], v[94:97], v[38:41]
	v_mfma_f32_16x16x32_f16 v[6:9], v[86:89], v[102:105], v[26:29]
	s_waitcnt lgkmcnt(1)
	v_mfma_f32_16x16x32_f16 v[22:25], v[110:113], v[98:101], v[22:25]
	v_mfma_f32_16x16x32_f16 v[26:29], v[110:113], v[106:109], v[50:53]
	s_waitcnt lgkmcnt(0)
	v_mfma_f32_16x16x32_f16 v[2:5], v[110:113], v[114:117], v[18:21]
	v_mfma_f32_16x16x32_f16 v[18:21], v[62:65], v[98:101], v[54:57]
	v_mfma_f32_16x16x32_f16 v[38:41], v[62:65], v[106:109], v[58:61]
	v_mfma_f32_16x16x32_f16 v[14:17], v[62:65], v[114:117], v[14:17]
	v_mfma_f32_16x16x32_f16 v[42:45], v[66:69], v[98:101], v[42:45]
	v_mfma_f32_16x16x32_f16 v[46:49], v[66:69], v[106:109], v[46:49]
	v_mfma_f32_16x16x32_f16 v[10:13], v[66:69], v[114:117], v[10:13]
	v_mfma_f32_16x16x32_f16 v[30:33], v[70:73], v[98:101], v[30:33]
	v_mfma_f32_16x16x32_f16 v[34:37], v[70:73], v[106:109], v[34:37]
	v_mfma_f32_16x16x32_f16 v[6:9], v[70:73], v[114:117], v[6:9]
	s_waitcnt vmcnt(0) lgkmcnt(0)
	s_barrier
	ds_read_b128 v[50:53], v78 offset:43008
	ds_read_b128 v[54:57], v78 offset:45056
	ds_read_b128 v[58:61], v78 offset:47104
	ds_read_b128 v[62:65], v82 offset:57344
	ds_read_b128 v[66:69], v82 offset:59392
	ds_read_b128 v[70:73], v78 offset:40960
	ds_read_b128 v[74:77], v82 offset:61440
	s_waitcnt lgkmcnt(1)
	v_mfma_f32_16x16x32_f16 v[22:25], v[70:73], v[62:65], v[22:25]
	v_mfma_f32_16x16x32_f16 v[26:29], v[70:73], v[66:69], v[26:29]
	s_waitcnt lgkmcnt(0)
	v_mfma_f32_16x16x32_f16 v[2:5], v[70:73], v[74:77], v[2:5]
	v_mfma_f32_16x16x32_f16 v[18:21], v[50:53], v[62:65], v[18:21]
	v_mfma_f32_16x16x32_f16 v[38:41], v[50:53], v[66:69], v[38:41]
	v_mfma_f32_16x16x32_f16 v[14:17], v[50:53], v[74:77], v[14:17]
	ds_read_b128 v[50:53], v78 offset:44032
	ds_read_b128 v[70:73], v78 offset:46080
	ds_read_b128 v[84:87], v78 offset:48128
	ds_read_b128 v[88:91], v82 offset:58368
	ds_read_b128 v[92:95], v82 offset:60416
	ds_read_b128 v[96:99], v78 offset:41984
	ds_read_b128 v[100:103], v82 offset:62464
	v_mfma_f32_16x16x32_f16 v[42:45], v[54:57], v[62:65], v[42:45]
	v_mfma_f32_16x16x32_f16 v[46:49], v[54:57], v[66:69], v[46:49]
	v_mfma_f32_16x16x32_f16 v[10:13], v[54:57], v[74:77], v[10:13]
	v_mfma_f32_16x16x32_f16 v[30:33], v[58:61], v[62:65], v[30:33]
	v_mfma_f32_16x16x32_f16 v[34:37], v[58:61], v[66:69], v[34:37]
	v_mfma_f32_16x16x32_f16 v[6:9], v[58:61], v[74:77], v[6:9]
	s_waitcnt lgkmcnt(1)
	v_mfma_f32_16x16x32_f16 v[22:25], v[96:99], v[88:91], v[22:25]
	v_mfma_f32_16x16x32_f16 v[26:29], v[96:99], v[92:95], v[26:29]
	s_waitcnt lgkmcnt(0)
	v_mfma_f32_16x16x32_f16 v[2:5], v[96:99], v[100:103], v[2:5]
	v_mfma_f32_16x16x32_f16 v[18:21], v[50:53], v[88:91], v[18:21]
	v_mfma_f32_16x16x32_f16 v[38:41], v[50:53], v[92:95], v[38:41]
	v_mfma_f32_16x16x32_f16 v[14:17], v[50:53], v[100:103], v[14:17]
	v_mfma_f32_16x16x32_f16 v[42:45], v[70:73], v[88:91], v[42:45]
	v_mfma_f32_16x16x32_f16 v[46:49], v[70:73], v[92:95], v[46:49]
	v_mfma_f32_16x16x32_f16 v[10:13], v[70:73], v[100:103], v[10:13]
	v_mfma_f32_16x16x32_f16 v[30:33], v[84:87], v[88:91], v[30:33]
	v_mfma_f32_16x16x32_f16 v[34:37], v[84:87], v[92:95], v[34:37]
	v_mfma_f32_16x16x32_f16 v[6:9], v[84:87], v[100:103], v[6:9]
	v_and_or_b32 v50, v80, 12, v81
	v_add_u32_e32 v50, s2, v50
	v_mul_u32_u24_e32 v1, 48, v1
	v_and_or_b32 v52, v0, 15, v1
	v_mul_u32_u24_e32 v0, 0xc00, v50
	v_mov_b32_e32 v1, 0
	v_lshl_add_u64 v[50:51], s[0:1], 0, v[0:1]
	v_add_lshl_u32 v0, v52, s8, 2
	v_lshl_add_u64 v[0:1], v[50:51], 0, v[0:1]
	s_mov_b64 s[0:1], 0x1800
	s_barrier
	global_store_dword v[0:1], v22, off
	global_store_dword v[0:1], v26, off offset:64
	global_store_dword v[0:1], v2, off offset:128
	global_store_dword v[0:1], v23, off offset:3072
	global_store_dword v[0:1], v27, off offset:3136
	global_store_dword v[0:1], v3, off offset:3200
	v_lshl_add_u64 v[2:3], v[0:1], 0, s[0:1]
	s_movk_i32 s0, 0x1000
	v_add_co_u32_e32 v22, vcc, s0, v0
	s_mov_b64 s[0:1], 0x2400
	s_nop 0
	v_addc_co_u32_e32 v23, vcc, 0, v1, vcc
	global_store_dword v[22:23], v24, off offset:2048
	global_store_dword v[2:3], v28, off offset:64
	global_store_dword v[2:3], v4, off offset:128
	v_lshl_add_u64 v[2:3], v[0:1], 0, s[0:1]
	s_movk_i32 s0, 0x2000
	v_add_co_u32_e32 v22, vcc, s0, v0
	s_mov_b64 s[0:1], 0xc000
	s_nop 0
	v_addc_co_u32_e32 v23, vcc, 0, v1, vcc
	global_store_dword v[22:23], v25, off offset:1024
	global_store_dword v[2:3], v29, off offset:64
	global_store_dword v[2:3], v5, off offset:128
	v_lshl_add_u64 v[2:3], v[0:1], 0, s[0:1]
	s_mov_b32 s0, 0xc000
	v_add_co_u32_e32 v4, vcc, s0, v0
	s_mov_b64 s[0:1], 0xcc00
	s_nop 0
	v_addc_co_u32_e32 v5, vcc, 0, v1, vcc
	global_store_dword v[4:5], v18, off
	global_store_dword v[2:3], v38, off offset:64
	global_store_dword v[2:3], v14, off offset:128
	v_lshl_add_u64 v[2:3], v[0:1], 0, s[0:1]
	s_mov_b64 s[0:1], 0xd800
	global_store_dword v[4:5], v19, off offset:3072
	global_store_dword v[2:3], v39, off offset:64
	global_store_dword v[2:3], v15, off offset:128
	v_lshl_add_u64 v[2:3], v[0:1], 0, s[0:1]
	s_mov_b32 s0, 0xd000
	v_add_co_u32_e32 v4, vcc, s0, v0
	s_mov_b64 s[0:1], 0xe400
	s_nop 0
	v_addc_co_u32_e32 v5, vcc, 0, v1, vcc
	global_store_dword v[4:5], v20, off offset:2048
	global_store_dword v[2:3], v40, off offset:64
	global_store_dword v[2:3], v16, off offset:128
	v_add_co_u32_e32 v4, vcc, s3, v0
	v_lshl_add_u64 v[2:3], v[0:1], 0, s[0:1]
	s_nop 0
	v_addc_co_u32_e32 v5, vcc, 0, v1, vcc
	s_mov_b64 s[0:1], 0x18000
	global_store_dword v[4:5], v21, off offset:1024
	global_store_dword v[2:3], v41, off offset:64
	global_store_dword v[2:3], v17, off offset:128
	v_lshl_add_u64 v[2:3], v[0:1], 0, s[0:1]
	s_mov_b32 s0, 0x18000
	v_add_co_u32_e32 v4, vcc, s0, v0
	s_mov_b64 s[0:1], 0x18c00
	s_nop 0
	v_addc_co_u32_e32 v5, vcc, 0, v1, vcc
	global_store_dword v[4:5], v42, off
	global_store_dword v[2:3], v46, off offset:64
	global_store_dword v[2:3], v10, off offset:128
	v_lshl_add_u64 v[2:3], v[0:1], 0, s[0:1]
	s_mov_b64 s[0:1], 0x19800
	global_store_dword v[4:5], v43, off offset:3072
	global_store_dword v[2:3], v47, off offset:64
	global_store_dword v[2:3], v11, off offset:128
	v_lshl_add_u64 v[2:3], v[0:1], 0, s[0:1]
	s_mov_b32 s0, 0x19000
	v_add_co_u32_e32 v4, vcc, s0, v0
	s_mov_b64 s[0:1], 0x1a400
	s_nop 0
	v_addc_co_u32_e32 v5, vcc, 0, v1, vcc
	global_store_dword v[4:5], v44, off offset:2048
	global_store_dword v[2:3], v48, off offset:64
	global_store_dword v[2:3], v12, off offset:128
	v_lshl_add_u64 v[2:3], v[0:1], 0, s[0:1]
	s_mov_b32 s0, 0x1a000
	v_add_co_u32_e32 v4, vcc, s0, v0
	s_mov_b64 s[0:1], 0x24000
	s_nop 0
	v_addc_co_u32_e32 v5, vcc, 0, v1, vcc
	global_store_dword v[4:5], v45, off offset:1024
	global_store_dword v[2:3], v49, off offset:64
	global_store_dword v[2:3], v13, off offset:128
	v_lshl_add_u64 v[2:3], v[0:1], 0, s[0:1]
	s_mov_b32 s0, 0x24000
	v_add_co_u32_e32 v4, vcc, s0, v0
	s_mov_b64 s[0:1], 0x24c00
	s_nop 0
	v_addc_co_u32_e32 v5, vcc, 0, v1, vcc
	global_store_dword v[4:5], v30, off
	global_store_dword v[2:3], v34, off offset:64
	global_store_dword v[2:3], v6, off offset:128
	v_lshl_add_u64 v[2:3], v[0:1], 0, s[0:1]
	s_mov_b64 s[0:1], 0x25800
	global_store_dword v[4:5], v31, off offset:3072
	global_store_dword v[2:3], v35, off offset:64
	global_store_dword v[2:3], v7, off offset:128
	v_lshl_add_u64 v[2:3], v[0:1], 0, s[0:1]
	s_mov_b32 s0, 0x25000
	v_add_co_u32_e32 v4, vcc, s0, v0
	s_mov_b64 s[0:1], 0x26400
	s_nop 0
	v_addc_co_u32_e32 v5, vcc, 0, v1, vcc
	global_store_dword v[4:5], v32, off offset:2048
	global_store_dword v[2:3], v36, off offset:64
	global_store_dword v[2:3], v8, off offset:128
	v_lshl_add_u64 v[2:3], v[0:1], 0, s[0:1]
	v_add_co_u32_e32 v0, vcc, 0x26000, v0
	s_nop 1
	v_addc_co_u32_e32 v1, vcc, 0, v1, vcc
	global_store_dword v[0:1], v33, off offset:1024
	global_store_dword v[2:3], v37, off offset:64
	global_store_dword v[2:3], v9, off offset:128
